# deferred weight-conversion split: 2600 + 1300 tiles deferred, idle-slot quotas 6/7/6/7
# speedup vs baseline: 1.0019x; 1.0019x over previous
; #define SEAM(k) do { if (IN(k) && IN((k) + 1)) xcd_barrier(bar); \
;         if (PROBE_MASK) { const unsigned long long t_ = __builtin_amdgcn_s_memrealtime(); if ((PROBE_MASK >> (k)) & 1u) pr_acc += t_ - pr_t0; pr_t0 = t_; } } while (0)
; __device__ __forceinline__ void convert_deferred(const Ptrs& P, unsigned char* lds, int quota) {
;     const int tid = threadIdx.x, wid = tid >> 6, lane = tid & 63;
;     float* tile = (float*)lds;
;     volatile __attribute__((address_space(3))) int* slot = (volatile __attribute__((address_space(3))) int*)((__attribute__((address_space(3))) unsigned char*)lds + 131072 + 320 + 11000);
;     unsigned* q = (unsigned*)(P.ws + WS_CTL) + CW_DEFQ;
;     for (int n = 0; n < quota; ++n) {
;         __syncthreads();
;         if (tid == 0) *slot = (int)atomicAdd(q, 1u);
;         __syncthreads();
;         const int t = *slot;
;         if (t >= DEF_GU + DEF_DN) break;
;         const bool gu = t < DEF_GU;
;         const float* src = gu ? P.in[34] : P.in[36]; bf16* dst = (bf16*)(P.ws + (gu ? WS_WGU : WS_WDN));
;         const int N = gu ? 2048 : 1024, ntn = N / 256, it = gu ? 2 * NE * 16 * 8 - DEF_GU + t : 2 * NE * 16 * 4 - DEF_DN + (t - DEF_GU);
; __global__ void __launch_bounds__(NT, 2) mega(Args args) {
;     ...
;     if (IN(6)) { g8::DenseOrder S; S.init(MIX, D, (const bf16*)(ws + WS_WEVOUT), D, R, D, G, (int)blockIdx.x, 0); g8::EpiOut E{P, 0};
;         g8::gemm_phase<g8::EpiOut, g8::DenseOrder, false, true>(LDSP, D, D, S, E);
;         if (IDLE_LAST(68 * 4)) convert_deferred(P, lds, 4); } SEAM(6);
.LBB0_1286:
	s_abs_i32 s3, s62
	v_cvt_f32_u32_e32 v2, s3
	s_sub_i32 s4, 0, s3
	s_mov_b32 s5, 0
	v_rcp_iflag_f32_e32 v2, v2
	s_nop 0
	v_mul_f32_e32 v2, 0x4f7ffffe, v2
	v_cvt_u32_f32_e32 v2, v2
	s_nop 0
	v_readfirstlane_b32 s6, v2
	s_mul_i32 s4, s4, s6
	s_mul_hi_u32 s4, s6, s4
	s_add_i32 s6, s6, s4
	s_mul_hi_u32 s4, s6, 0x110
	s_mul_i32 s4, s4, s3
	s_sub_i32 s4, 0x110, s4
	s_sub_i32 s6, s4, s3
	s_cmp_ge_u32 s4, s3
	s_cselect_b32 s4, s6, s4
	s_sub_i32 s6, s4, s3
	s_cmp_ge_u32 s4, s3
	s_cselect_b32 s3, s6, s4
	s_cmp_eq_u32 s3, 0
	s_cselect_b64 s[6:7], -1, 0
	s_cmp_lt_i32 s2, s3
	s_cselect_b64 s[8:9], -1, 0
	s_or_b64 s[6:7], s[6:7], s[8:9]
	s_and_b64 vcc, exec, s[6:7]
	s_cbranch_vccnz .LBB0_1296
	v_and_b32_e32 v2, 0x7c, v188
	v_lshlrev_b32_e32 v3, 5, v0
	s_movk_i32 s3, 0x400
	v_and_or_b32 v12, v3, s3, v2
	v_bfe_u32 v2, v0, 3, 3
	v_lshl_or_b32 v4, v1, 5, v2
	v_lshlrev_b32_e32 v2, 3, v0
	v_lshl_add_u32 v11, v182, 4, 0
	v_and_b32_e32 v2, 56, v2
	v_mul_u32_u24_e32 v16, 0x2020, v1
	v_mov_b32_e32 v3, 0
	v_lshl_add_u32 v27, v4, 2, 0
	v_mul_u32_u24_e32 v28, 0x404, v2
	v_lshlrev_b32_e32 v10, 6, v4
	s_add_i32 s12, 0, 0x22c38
	v_add_u32_e32 v16, v11, v16
	v_and_b32_e32 v13, 0xfc, v188
	v_and_b32_e32 v14, 56, v185
	s_mov_b32 s3, 7
	v_or_b32_e32 v4, 0x200, v10
	v_mov_b32_e32 v5, v3
	v_or_b32_e32 v6, 0x400, v10
	v_mov_b32_e32 v7, v3
	v_or_b32_e32 v8, 0x600, v10
	v_mov_b32_e32 v9, v3
	v_mov_b32_e32 v15, s12
	s_movk_i32 s13, 0xf3b
	s_movk_i32 s14, 0x800
	s_mov_b32 s15, 0x1104e000
	s_movk_i32 s16, 0xc4
	v_add_u32_e32 v17, 0x404, v16
	v_add_u32_e32 v18, 0x40c, v16
	v_add_u32_e32 v19, 0x808, v16
	v_add_u32_e32 v20, 0xc0c, v16
	v_add_u32_e32 v21, 0xc14, v16
	v_add_u32_e32 v22, 0x1414, v16
	v_add_u32_e32 v23, 0x141c, v16
	v_add_u32_e32 v24, 0x1818, v16
	v_add_u32_e32 v25, 0x1c1c, v16
	v_add_u32_e32 v26, 0x1c24, v16
	v_lshlrev_b32_e32 v2, 1, v2
	v_add_u32_e32 v27, v27, v28
	v_lshlrev_b32_e32 v10, 1, v10
	s_branch .LBB0_1289

; #define LAS __attribute__((address_space(3)))
; #define SEAM(k) do { if (IN(k) && IN((k) + 1)) xcd_barrier(bar); \
;         if (PROBE_MASK) { const unsigned long long t_ = __builtin_amdgcn_s_memrealtime(); if ((PROBE_MASK >> (k)) & 1u) pr_acc += t_ - pr_t0; pr_t0 = t_; } } while (0)
; __device__ __forceinline__ void convert_deferred(const Ptrs& P, unsigned char* lds, int quota) {
;     const int tid = threadIdx.x, wid = tid >> 6, lane = tid & 63;
;     float* tile = (float*)lds;
;     volatile __attribute__((address_space(3))) int* slot = (volatile __attribute__((address_space(3))) int*)((__attribute__((address_space(3))) unsigned char*)lds + 131072 + 320 + 11000);
;     unsigned* q = (unsigned*)(P.ws + WS_CTL) + CW_DEFQ;
;     for (int n = 0; n < quota; ++n) {
;         __syncthreads();
;         if (tid == 0) *slot = (int)atomicAdd(q, 1u);
;         __syncthreads();
;         const int t = *slot;
;         if (t >= DEF_GU + DEF_DN) break;
;         const bool gu = t < DEF_GU;
;         const float* src = gu ? P.in[34] : P.in[36]; bf16* dst = (bf16*)(P.ws + (gu ? WS_WGU : WS_WDN));
;         const int N = gu ? 2048 : 1024, ntn = N / 256, it = gu ? 2 * NE * 16 * 8 - DEF_GU + t : 2 * NE * 16 * 4 - DEF_DN + (t - DEF_GU);
; __global__ void __launch_bounds__(NT, 2) mega(Args args) {
;     ...
;     if (IN(9)) { g8::MoeOrder S{(const char*)(ws + WS_ACT), (const char*)(ws + WS_WDN) + (size_t)0 * NE * 1024 * 1024 * 2, nullptr, (size_t)1024 * 1024 * 2, 4, D, G, vcu, 0, nullptr};
;         S.init((const unsigned*)(ws + WS_CTL) + CW_CNT + 0 * 64, (LAS int*)(LDSP + MISC_OFF + 256)); g8::EpiMoe2 E{P, 0}; g8::gemm_phase<g8::EpiMoe2, g8::MoeOrder, false, true>(LDSP, D, D, S, E);
;         { const int rem_ = ((LAS int*)(LDSP + MISC_OFF + 256))[96] % G; if (rem_ != 0 && vcu >= rem_) convert_deferred(P, lds, 5); } } SEAM(9);
.LBB0_1609:
	s_abs_i32 s0, s62
	v_cvt_f32_u32_e32 v2, s0
	s_sub_i32 s5, 0, s0
	s_abs_i32 s4, s9
	s_ashr_i32 s3, s9, 31
	v_rcp_iflag_f32_e32 v2, v2
	s_mov_b32 s1, 0
	v_mul_f32_e32 v2, 0x4f7ffffe, v2
	v_cvt_u32_f32_e32 v2, v2
	s_nop 0
	v_readfirstlane_b32 s6, v2
	s_mul_i32 s5, s5, s6
	s_mul_hi_u32 s5, s6, s5
	s_add_i32 s6, s6, s5
	s_mul_hi_u32 s5, s4, s6
	s_mul_i32 s5, s5, s0
	s_sub_i32 s4, s4, s5
	s_sub_i32 s5, s4, s0
	s_cmp_ge_u32 s4, s0
	s_cselect_b32 s4, s5, s4
	s_sub_i32 s5, s4, s0
	s_cmp_ge_u32 s4, s0
	s_cselect_b32 s0, s5, s4
	s_xor_b32 s0, s0, s3
	s_sub_i32 s0, s0, s3
	s_cmp_eq_u32 s0, 0
	v_readlane_b32 s3, v254, 2
	s_cselect_b64 s[4:5], -1, 0
	s_cmp_lt_i32 s3, s0
	s_cselect_b64 s[6:7], -1, 0
	s_or_b64 s[4:5], s[4:5], s[6:7]
	s_and_b64 vcc, exec, s[4:5]
	s_cbranch_vccnz .LBB0_1619
	v_and_b32_e32 v2, 0x7c, v175
	v_lshlrev_b32_e32 v3, 5, v0
	s_movk_i32 s0, 0x400
	v_and_or_b32 v12, v3, s0, v2
	v_bfe_u32 v2, v0, 3, 3
	v_lshl_or_b32 v4, v1, 5, v2
	v_lshlrev_b32_e32 v2, 3, v0
	v_lshl_add_u32 v11, v182, 4, 0
	v_and_b32_e32 v2, 56, v2
	v_mul_u32_u24_e32 v16, 0x2020, v1
	v_mov_b32_e32 v3, 0
	v_lshl_add_u32 v27, v4, 2, 0
	v_mul_u32_u24_e32 v28, 0x404, v2
	v_lshlrev_b32_e32 v10, 6, v4
	s_add_i32 s10, 0, 0x22c38
	v_add_u32_e32 v16, v11, v16
	s_mov_b32 s3, 6
	v_and_b32_e32 v13, 0xfc, v175
	v_and_b32_e32 v14, 56, v173
	v_or_b32_e32 v4, 0x200, v10
	v_mov_b32_e32 v5, v3
	v_or_b32_e32 v6, 0x400, v10
	v_mov_b32_e32 v7, v3
	v_or_b32_e32 v8, 0x600, v10
	v_mov_b32_e32 v9, v3
	v_mov_b32_e32 v15, s10
	s_movk_i32 s11, 0xf3b
	s_movk_i32 s12, 0x800
	s_mov_b32 s13, 0x1104e000
	s_movk_i32 s14, 0xc4
	v_add_u32_e32 v17, 0x404, v16
	v_add_u32_e32 v18, 0x40c, v16
	v_add_u32_e32 v19, 0x808, v16
	v_add_u32_e32 v20, 0xc0c, v16
	v_add_u32_e32 v21, 0xc14, v16
	v_add_u32_e32 v22, 0x1414, v16
	v_add_u32_e32 v23, 0x141c, v16
	v_add_u32_e32 v24, 0x1818, v16
	v_add_u32_e32 v25, 0x1c1c, v16
	v_add_u32_e32 v26, 0x1c24, v16
	v_lshlrev_b32_e32 v2, 1, v2
	v_add_u32_e32 v27, v27, v28
	v_lshlrev_b32_e32 v10, 1, v10
	s_branch .LBB0_1612

; #define LAS __attribute__((address_space(3)))
; #define SEAM(k) do { if (IN(k) && IN((k) + 1)) xcd_barrier(bar); \
;         if (PROBE_MASK) { const unsigned long long t_ = __builtin_amdgcn_s_memrealtime(); if ((PROBE_MASK >> (k)) & 1u) pr_acc += t_ - pr_t0; pr_t0 = t_; } } while (0)
; __device__ __forceinline__ void convert_deferred(const Ptrs& P, unsigned char* lds, int quota) {
;     const int tid = threadIdx.x, wid = tid >> 6, lane = tid & 63;
;     float* tile = (float*)lds;
;     volatile __attribute__((address_space(3))) int* slot = (volatile __attribute__((address_space(3))) int*)((__attribute__((address_space(3))) unsigned char*)lds + 131072 + 320 + 11000);
;     unsigned* q = (unsigned*)(P.ws + WS_CTL) + CW_DEFQ;
;     for (int n = 0; n < quota; ++n) {
;         __syncthreads();
;         if (tid == 0) *slot = (int)atomicAdd(q, 1u);
;         __syncthreads();
;         const int t = *slot;
;         if (t >= DEF_GU + DEF_DN) break;
;         const bool gu = t < DEF_GU;
;         const float* src = gu ? P.in[34] : P.in[36]; bf16* dst = (bf16*)(P.ws + (gu ? WS_WGU : WS_WDN));
;         const int N = gu ? 2048 : 1024, ntn = N / 256, it = gu ? 2 * NE * 16 * 8 - DEF_GU + t : 2 * NE * 16 * 4 - DEF_DN + (t - DEF_GU);
; __global__ void __launch_bounds__(NT, 2) mega(Args args) {
;     ...
;     if (IN(11)) { g8::DenseOrder S; S.init(H, D, (const bf16*)(ws + WS_WODIN), D, R, ODD_IN, G, (int)blockIdx.x, 0);
;         g8::EpiDiffIn E{Z, P.in[25], P.in[26], (const float*)(ws + WS_ROPE), (const float*)(ws + WS_ROPE) + SEQ * 64, (LAS float*)(LDSP + MISC_OFF + 1024)};
;         g8::gemm_phase<g8::EpiDiffIn, g8::DenseOrder, false, true>(LDSP, D, D, S, E);
;         if (IDLE_LAST(68 * 12)) convert_deferred(P, lds, 4); } SEAM(11);
.LBB0_1851:
	s_abs_i32 s0, s62
	v_cvt_f32_u32_e32 v2, s0
	s_sub_i32 s3, 0, s0
	v_readlane_b32 s56, v254, 40
	s_mov_b32 s1, 0
	v_rcp_iflag_f32_e32 v2, v2
	v_readlane_b32 s57, v254, 41
	v_mul_f32_e32 v2, 0x4f7ffffe, v2
	v_cvt_u32_f32_e32 v2, v2
	s_nop 0
	v_readfirstlane_b32 s4, v2
	s_mul_i32 s3, s3, s4
	s_mul_hi_u32 s3, s4, s3
	s_add_i32 s4, s4, s3
	s_mul_hi_u32 s3, s4, 0x330
	s_mul_i32 s3, s3, s0
	s_sub_i32 s3, 0x330, s3
	s_sub_i32 s4, s3, s0
	s_cmp_ge_u32 s3, s0
	s_cselect_b32 s3, s4, s3
	s_sub_i32 s4, s3, s0
	s_cmp_ge_u32 s3, s0
	s_cselect_b32 s0, s4, s3
	s_cmp_eq_u32 s0, 0
	s_cselect_b64 s[4:5], -1, 0
	s_cmp_lt_i32 s2, s0
	s_cselect_b64 s[6:7], -1, 0
	s_or_b64 s[4:5], s[4:5], s[6:7]
	s_and_b64 vcc, exec, s[4:5]
	s_cbranch_vccnz .LBB0_1861
	v_and_b32_e32 v2, 0x7c, v218
	v_lshlrev_b32_e32 v3, 5, v0
	s_movk_i32 s0, 0x400
	v_and_or_b32 v12, v3, s0, v2
	v_bfe_u32 v2, v0, 3, 3
	v_lshl_or_b32 v4, v1, 5, v2
	v_lshlrev_b32_e32 v2, 3, v0
	v_lshl_add_u32 v11, v182, 4, 0
	v_and_b32_e32 v2, 56, v2
	v_mul_u32_u24_e32 v16, 0x2020, v1
	v_mov_b32_e32 v3, 0
	s_waitcnt vmcnt(0)
	v_lshl_add_u32 v27, v4, 2, 0
	v_mul_u32_u24_e32 v28, 0x404, v2
	v_lshlrev_b32_e32 v10, 6, v4
	s_add_i32 s10, 0, 0x22c38
	v_add_u32_e32 v16, v11, v16
	v_and_b32_e32 v13, 0xfc, v218
	v_and_b32_e32 v14, 56, v179
	s_mov_b32 s3, 7
	v_or_b32_e32 v4, 0x200, v10
	v_mov_b32_e32 v5, v3
	v_or_b32_e32 v6, 0x400, v10
	v_mov_b32_e32 v7, v3
	v_or_b32_e32 v8, 0x600, v10
	v_mov_b32_e32 v9, v3
	v_mov_b32_e32 v15, s10
	s_movk_i32 s11, 0xf3b
	s_movk_i32 s12, 0x800
	s_mov_b32 s13, 0x1104e000
	s_movk_i32 s14, 0xc4
	v_add_u32_e32 v17, 0x404, v16
	v_add_u32_e32 v18, 0x40c, v16
	v_add_u32_e32 v19, 0x808, v16
	v_add_u32_e32 v20, 0xc0c, v16
	v_add_u32_e32 v21, 0xc14, v16
	v_add_u32_e32 v22, 0x1414, v16
	v_add_u32_e32 v23, 0x141c, v16
	v_add_u32_e32 v24, 0x1818, v16
	v_add_u32_e32 v25, 0x1c1c, v16
	v_add_u32_e32 v26, 0x1c24, v16
	v_lshlrev_b32_e32 v2, 1, v2
	v_add_u32_e32 v27, v27, v28
	v_lshlrev_b32_e32 v10, 1, v10
	s_branch .LBB0_1854
